# speedup vs baseline: 1.0062x; 1.0034x over previous
.LBB0_9:
	s_or_b64 exec, exec, s[8:9]
	v_add_u32_e32 v35, 0x5000, v27
	v_add_u32_e32 v34, 0x5000, v28
	v_add_u32_e32 v30, 0x5000, v30
	v_add_u32_e32 v28, 0x5000, v31
	v_add_u32_e32 v27, 0x5000, v32
	s_barrier
	s_and_saveexec_b64 s[4:5], vcc
	s_cbranch_execz .LBB0_12
	s_load_dwordx2 s[8:9], s[0:1], 0x10
	s_movk_i32 s3, 0x7d
	v_mov_b32_e32 v31, s2
	v_mad_u32_u24 v32, v0, s3, v31
	v_sub_u32_e32 v29, v33, v29
	v_ashrrev_i32_e32 v33, 31, v32
	s_waitcnt lgkmcnt(0)
	v_lshl_add_u64 v[32:33], v[32:33], 2, s[8:9]
	v_cmp_eq_u32_e32 vcc, 0, v0
	ds_write_b32 v1, v29 offset:20480
	global_store_dword v[32:33], v29, off sc0 sc1
	s_and_b64 exec, exec, vcc
	s_cbranch_execz .LBB0_12
	s_ashr_i32 s3, s2, 31
	s_lshl_b64 s[10:11], s[2:3], 2
	s_add_u32 s8, s8, s10
	s_addc_u32 s9, s9, s11
	v_mov_b32_e32 v29, 0x1f000
	v_mov_b32_e32 v31, 0x1400
	global_store_dword v29, v31, s[8:9] offset:1024 sc0 sc1
.LBB0_12:
	s_or_b64 exec, exec, s[4:5]
	v_mov_b32_e32 v29, 1
	s_waitcnt lgkmcnt(0)
	s_barrier
	ds_add_rtn_u32 v31, v35, v29
	s_mov_b32 s3, 0xff3c
	v_mad_u64_u32 v[32:33], s[4:5], v26, s3, v[12:13]
	v_lshl_or_b32 v12, v32, 16, v13
	s_waitcnt lgkmcnt(0)
	v_lshlrev_b32_e32 v13, 2, v31
	ds_write_b32 v13, v12
	ds_add_rtn_u32 v26, v34, v29
	v_mad_u64_u32 v[12:13], s[4:5], v25, s3, v[14:15]
	v_lshl_or_b32 v12, v12, 16, v15
	v_lshl_add_u64 v[2:3], v[2:3], 2, s[6:7]
	s_waitcnt lgkmcnt(0)
	v_lshlrev_b32_e32 v13, 2, v26
	ds_write_b32 v13, v12
	ds_add_rtn_u32 v14, v30, v29
	v_mad_u64_u32 v[12:13], s[4:5], v24, s3, v[16:17]
	v_lshl_or_b32 v12, v12, 16, v17
	v_lshl_add_u64 v[4:5], v[4:5], 2, s[6:7]
	s_waitcnt lgkmcnt(0)
	v_lshlrev_b32_e32 v13, 2, v14
	ds_write_b32 v13, v12
	ds_add_rtn_u32 v14, v28, v29
	v_mad_u64_u32 v[12:13], s[4:5], v23, s3, v[18:19]
	v_lshl_or_b32 v12, v12, 16, v19
	s_waitcnt lgkmcnt(0)
	v_lshlrev_b32_e32 v13, 2, v14
	ds_write_b32 v13, v12
	ds_add_rtn_u32 v14, v27, v29
	v_mad_u64_u32 v[12:13], s[4:5], v22, s3, v[20:21]
	v_lshl_or_b32 v12, v12, 16, v21
	s_mov_b64 s[4:5], 0
	s_waitcnt lgkmcnt(0)
	v_lshlrev_b32_e32 v13, 2, v14
	ds_write_b32 v13, v12
	s_waitcnt lgkmcnt(0)
	s_barrier
	ds_read2st64_b32 v[12:13], v1 offset1:16
	s_waitcnt lgkmcnt(0)
	global_store_dword v[2:3], v12, off sc0 sc1
	ds_read2st64_b32 v[2:3], v1 offset0:32 offset1:48
	ds_read_b32 v1, v1 offset:16384
	global_store_dword v[4:5], v13, off sc0 sc1
	v_lshl_add_u64 v[4:5], v[6:7], 2, s[6:7]
	s_waitcnt lgkmcnt(1)
	global_store_dword v[4:5], v2, off sc0 sc1
	v_lshl_add_u64 v[4:5], v[8:9], 2, s[6:7]
	global_store_dword v[4:5], v3, off sc0 sc1
	v_lshl_add_u64 v[2:3], v[10:11], 2, s[6:7]
	s_waitcnt lgkmcnt(0)
	global_store_dword v[2:3], v1, off sc0 sc1

.LBB0_17:
	v_lshrrev_b32_e32 v3, 3, v7
	v_lshrrev_b32_e32 v20, 3, v6
	v_ashrrev_i32_e32 v21, 7, v7
	v_ashrrev_i32_e32 v22, 7, v6
	v_lshrrev_b32_e32 v23, 5, v7
	v_lshrrev_b32_e32 v24, 5, v6
	v_and_b32_e32 v21, 0xffffffe0, v21
	v_and_b32_e32 v22, 0xffffffe0, v22
	v_and_b32_e32 v3, 31, v3
	v_and_b32_e32 v20, 31, v20
	v_and_b32_e32 v25, 0x70, v23
	v_and_b32_e32 v26, 0x70, v24
	v_and_b32_e32 v23, 8, v23
	v_and_b32_e32 v24, 8, v24
	v_or_b32_e32 v3, v21, v3
	v_or_b32_e32 v20, v22, v20
	v_or_b32_e32 v21, v23, v1
	v_or_b32_e32 v22, v24, v4
	v_or_b32_e32 v21, v21, v25
	v_or_b32_e32 v22, v22, v26
	v_lshlrev_b32_e32 v23, 6, v3
	v_lshlrev_b32_e32 v24, 6, v20
	v_lshlrev_b32_e32 v27, 7, v20
	v_lshlrev_b32_e32 v3, 7, v3
	v_add3_u32 v28, v21, v23, s25
	v_or_b32_e32 v23, v23, v21
	v_cmp_gt_u32_e32 vcc, 64, v25
	v_add3_u32 v25, v22, v24, s25
	v_or_b32_e32 v24, v24, v22
	v_or_b32_e32 v22, v27, v22
	v_cmp_gt_u32_e64 s[2:3], 64, v26
	v_or_b32_e32 v20, v3, v21
	v_cndmask_b32_e32 v26, v28, v23, vcc
	v_cndmask_b32_e64 v24, v25, v24, s[2:3]
	v_ashrrev_i32_e32 v23, 31, v22
	v_cndmask_b32_e32 v29, v11, v12, vcc
	v_cndmask_b32_e32 v28, v13, v14, vcc
	v_cndmask_b32_e64 v31, v15, v16, s[2:3]
	v_cndmask_b32_e64 v30, v17, v18, s[2:3]
	v_ashrrev_i32_e32 v21, 31, v20
	v_ashrrev_i32_e32 v27, 31, v26
	v_ashrrev_i32_e32 v25, 31, v24
	v_lshl_add_u64 v[22:23], v[22:23], 2, s[16:17]
	v_lshl_add_u64 v[20:21], v[20:21], 2, s[16:17]
	v_lshl_add_u64 v[24:25], v[24:25], 2, v[30:31]
	v_lshl_add_u64 v[26:27], v[26:27], 2, v[28:29]
	global_load_dword v3, v[22:23], off nt
	global_load_dword v28, v[20:21], off nt
	global_load_dword v29, v[24:25], off nt
	global_load_dword v30, v[26:27], off nt
	v_ashrrev_i32_e32 v23, 31, v6
	v_mov_b32_e32 v22, v6
	v_add_u32_e32 v19, -2, v19
	v_ashrrev_i32_e32 v21, 31, v7
	v_mov_b32_e32 v20, v7
	v_lshlrev_b64 v[22:23], 1, v[22:23]
	v_cmp_eq_u32_e32 vcc, 0, v19
	v_add_u32_e32 v7, s24, v7
	v_add_u32_e32 v6, s13, v6
	v_lshlrev_b64 v[20:21], 1, v[20:21]
	v_lshl_add_u64 v[24:25], s[4:5], 0, v[22:23]
	v_lshl_add_u64 v[22:23], s[6:7], 0, v[22:23]
	s_or_b64 s[20:21], vcc, s[20:21]
	v_lshl_add_u64 v[26:27], s[4:5], 0, v[20:21]
	v_lshl_add_u64 v[20:21], s[6:7], 0, v[20:21]
	s_waitcnt vmcnt(2)
	v_cvt_pk_f16_f32 v3, v3, v28
	s_waitcnt vmcnt(0)
	v_cvt_pk_f16_f32 v28, v29, v30
	global_store_short v[22:23], v3, off sc0 sc1
	global_store_short_d16_hi v[20:21], v3, off sc0 sc1
	global_store_short v[24:25], v28, off sc0 sc1
	global_store_short_d16_hi v[26:27], v28, off sc0 sc1
	s_andn2_b64 exec, exec, s[20:21]
	s_cbranch_execnz .LBB0_17
	s_or_b64 exec, exec, s[20:21]
	v_mad_u64_u32 v[6:7], s[2:3], v9, s12, v[2:3]
	v_cmp_ne_u32_e32 vcc, v8, v9
	s_orn2_b64 s[2:3], vcc, exec

.LBB0_21:
	v_lshrrev_b32_e32 v12, 3, v6
	v_ashrrev_i32_e32 v13, 7, v6
	v_lshrrev_b32_e32 v14, 5, v6
	v_bfi_b32 v12, s13, v13, v12
	v_and_b32_e32 v13, 0x70, v14
	v_and_b32_e32 v14, 8, v14
	v_or3_b32 v14, v14, v4, v13
	v_lshlrev_b32_e32 v15, 6, v12
	v_add3_u32 v16, v14, v15, s20
	v_or_b32_e32 v15, v15, v14
	v_lshl_or_b32 v12, v12, 7, v14
	v_cmp_gt_u32_e32 vcc, 64, v13
	v_ashrrev_i32_e32 v13, 31, v12
	v_lshl_add_u64 v[12:13], v[12:13], 2, s[16:17]
	v_cndmask_b32_e32 v14, v16, v15, vcc
	v_cndmask_b32_e32 v17, v1, v3, vcc
	v_cndmask_b32_e32 v16, v7, v11, vcc
	v_ashrrev_i32_e32 v15, 31, v14
	v_lshl_add_u64 v[14:15], v[14:15], 2, v[16:17]
	global_load_dword v16, v[12:13], off nt
	global_load_dword v17, v[14:15], off nt
	v_add_u32_e32 v6, s12, v6
	v_cmp_lt_i32_e32 vcc, s8, v6
	v_lshl_add_u64 v[12:13], s[4:5], 0, v[8:9]
	v_lshl_add_u64 v[14:15], s[6:7], 0, v[8:9]
	v_lshl_add_u64 v[8:9], v[8:9], 0, s[2:3]
	s_or_b64 s[18:19], vcc, s[18:19]
	s_waitcnt vmcnt(1)
	v_cvt_f16_f32_e32 v16, v16
	s_waitcnt vmcnt(0)
	v_cvt_f16_f32_e32 v17, v17
	global_store_short v[14:15], v16, off sc0 sc1
	global_store_short v[12:13], v17, off sc0 sc1
	s_andn2_b64 exec, exec, s[18:19]
	s_cbranch_execnz .LBB0_21
.LBB0_22:
	s_or_b64 exec, exec, s[14:15]
	s_movk_i32 s2, 0x80
	v_cmp_gt_i32_e32 vcc, s2, v2
	s_and_saveexec_b64 s[2:3], vcc
	s_cbranch_execz .LBB0_24
	s_waitcnt lgkmcnt(0)
	s_load_dwordx4 s[4:7], s[0:1], 0x38
	v_mov_b32_e32 v3, 0
	v_lshlrev_b64 v[6:7], 2, v[2:3]
	s_waitcnt lgkmcnt(0)
	v_lshl_add_u64 v[12:13], s[4:5], 0, v[6:7]
	v_lshl_add_u64 v[8:9], s[6:7], 0, v[6:7]
	global_load_dword v1, v[12:13], off nt
	global_load_dword v3, v[8:9], off nt
	s_load_dwordx2 s[4:5], s[0:1], 0x58
	s_waitcnt lgkmcnt(0)
	v_lshl_add_u64 v[6:7], s[4:5], 0, v[6:7]
	s_waitcnt vmcnt(0)
	v_add_f32_e32 v1, v1, v3
	global_store_dword v[6:7], v1, off sc0 sc1

.LBB0_27:
	v_add_u32_e32 v7, -2, v7
	v_ashrrev_i32_e32 v9, 31, v1
	v_mov_b32_e32 v8, v1
	v_ashrrev_i32_e32 v11, 31, v0
	v_mov_b32_e32 v10, v0
	v_cmp_eq_u32_e32 vcc, 0, v7
	v_add_u32_e32 v1, s11, v1
	v_add_u32_e32 v0, s10, v0
	s_waitcnt lgkmcnt(0)
	v_lshl_add_u64 v[10:11], v[10:11], 2, s[6:7]
	v_lshl_add_u64 v[8:9], v[8:9], 2, s[6:7]
	s_or_b64 s[8:9], vcc, s[8:9]
	global_store_dword v[10:11], v6, off sc0 sc1
	global_store_dword v[8:9], v6, off sc0 sc1
	s_andn2_b64 exec, exec, s[8:9]
	s_cbranch_execnz .LBB0_27
	s_or_b64 exec, exec, s[8:9]
	v_mad_u64_u32 v[0:1], s[8:9], v5, s12, v[2:3]
	v_cmp_ne_u32_e32 vcc, v4, v5
	s_orn2_b64 s[8:9], vcc, exec

.LBB0_31:
	v_add_u32_e32 v0, s12, v0
	v_cmp_lt_i32_e32 vcc, s8, v0
	global_store_dword v[4:5], v1, off sc0 sc1
	s_or_b64 s[6:7], vcc, s[6:7]
	v_lshl_add_u64 v[4:5], v[4:5], 0, s[2:3]
	s_andn2_b64 exec, exec, s[6:7]
	s_cbranch_execnz .LBB0_31
.LBB0_32:
	s_or_b64 exec, exec, s[4:5]
	v_cmp_gt_i32_e32 vcc, 64, v2
	s_and_saveexec_b64 s[2:3], vcc
	s_cbranch_execz .LBB0_34
	s_load_dwordx2 s[4:5], s[0:1], 0x68
	v_mov_b32_e32 v3, 0
	s_waitcnt lgkmcnt(0)
	v_lshl_add_u64 v[0:1], v[2:3], 1, s[4:5]
	v_add_co_u32_e32 v0, vcc, 0x61a000, v0
	s_nop 1
	v_addc_co_u32_e32 v1, vcc, 0, v1, vcc
	global_store_short v[0:1], v3, off offset:2048 sc0 sc1
.LBB0_34:
	s_or_b64 exec, exec, s[2:3]
	v_cmp_gt_i32_e32 vcc, 32, v2
	s_and_saveexec_b64 s[2:3], vcc
	s_cbranch_execz .LBB0_36
	s_load_dwordx2 s[0:1], s[0:1], 0x70
	v_mov_b32_e32 v3, 0
	s_waitcnt lgkmcnt(0)
	v_lshl_add_u64 v[0:1], v[2:3], 2, s[0:1]
	v_add_co_u32_e32 v0, vcc, 0x61a000, v0
	s_nop 1
	v_addc_co_u32_e32 v1, vcc, 0, v1, vcc
	global_store_dword v[0:1], v3, off offset:2048 sc0 sc1

.LBB1_24:
	s_or_b64 exec, exec, s[12:13]
	v_mov_b32_e32 v18, 0
	s_waitcnt lgkmcnt(0)
	s_barrier
	ds_read_b64 v[30:31], v18 offset:22528
	s_and_saveexec_b64 s[10:11], s[8:9]
	v_lshlrev_b32_e32 v18, 2, v0
	ds_read_b32 v18, v18 offset:16384
	s_or_b64 exec, exec, s[10:11]
	v_mbcnt_lo_u32_b32 v19, -1, 0
	v_mbcnt_hi_u32_b32 v21, -1, v19
	v_and_b32_e32 v20, 64, v21
	v_add_u32_e32 v19, -1, v21
	v_cmp_lt_i32_e64 s[10:11], v19, v20
	v_and_b32_e32 v38, 63, v0
	v_add_u32_e32 v39, -2, v21
	v_cndmask_b32_e64 v19, v19, v21, s[10:11]
	v_lshlrev_b32_e32 v19, 2, v19
	s_waitcnt lgkmcnt(0)
	ds_bpermute_b32 v19, v19, v18
	v_cmp_ne_u32_e64 s[10:11], 0, v38
	s_waitcnt lgkmcnt(0)
	s_nop 0
	v_cndmask_b32_e64 v19, 0, v19, s[10:11]
	v_cmp_lt_i32_e64 s[10:11], v39, v20
	v_add_u32_e32 v19, v19, v18
	s_nop 0
	v_cndmask_b32_e64 v39, v39, v21, s[10:11]
	v_lshlrev_b32_e32 v39, 2, v39
	ds_bpermute_b32 v39, v39, v19
	v_cmp_lt_u32_e64 s[10:11], 1, v38
	s_waitcnt lgkmcnt(0)
	s_nop 0
	v_cndmask_b32_e64 v39, 0, v39, s[10:11]
	v_add_u32_e32 v19, v39, v19
	v_add_u32_e32 v39, -4, v21
	v_cmp_lt_i32_e64 s[10:11], v39, v20
	s_nop 1
	v_cndmask_b32_e64 v39, v39, v21, s[10:11]
	v_lshlrev_b32_e32 v39, 2, v39
	ds_bpermute_b32 v39, v39, v19
	v_cmp_lt_u32_e64 s[10:11], 3, v38
	s_waitcnt lgkmcnt(0)
	s_nop 0
	v_cndmask_b32_e64 v39, 0, v39, s[10:11]
	v_add_u32_e32 v19, v39, v19
	v_add_u32_e32 v39, -8, v21
	v_cmp_lt_i32_e64 s[10:11], v39, v20
	s_nop 1
	v_cndmask_b32_e64 v39, v39, v21, s[10:11]
	v_lshlrev_b32_e32 v39, 2, v39
	ds_bpermute_b32 v39, v39, v19
	v_cmp_lt_u32_e64 s[10:11], 7, v38
	s_waitcnt lgkmcnt(0)
	s_nop 0
	v_cndmask_b32_e64 v39, 0, v39, s[10:11]
	v_add_u32_e32 v19, v39, v19
	v_add_u32_e32 v39, -16, v21
	v_cmp_lt_i32_e64 s[10:11], v39, v20
	s_nop 1
	v_cndmask_b32_e64 v39, v39, v21, s[10:11]
	v_lshlrev_b32_e32 v39, 2, v39
	ds_bpermute_b32 v39, v39, v19
	v_cmp_lt_u32_e64 s[10:11], 15, v38
	s_waitcnt lgkmcnt(0)
	s_nop 0
	v_cndmask_b32_e64 v39, 0, v39, s[10:11]
	v_add_u32_e32 v19, v39, v19
	v_subrev_u32_e32 v39, 32, v21
	v_cmp_lt_i32_e64 s[10:11], v39, v20
	s_nop 1
	v_cndmask_b32_e64 v39, v39, v21, s[10:11]
	v_lshlrev_b32_e32 v39, 2, v39
	ds_bpermute_b32 v39, v39, v19
	v_cmp_gt_u32_e64 s[10:11], 32, v38
	s_waitcnt lgkmcnt(0)
	s_nop 0
	v_cndmask_b32_e64 v39, v39, 0, s[10:11]
	v_add_u32_e32 v19, v39, v19
	v_and_b32_e32 v39, 0x33f, v0
	v_cmp_eq_u32_e64 s[12:13], 63, v39
	s_and_saveexec_b64 s[14:15], s[12:13]
	v_and_b32_e32 v39, 60, v25
	ds_write_b32 v39, v19 offset:20480
	s_or_b64 exec, exec, s[14:15]
	s_waitcnt lgkmcnt(0)
	s_barrier
	s_and_saveexec_b64 s[18:19], s[8:9]
	s_cbranch_execz .LBB1_31
	v_mov_b32_e32 v39, 0
	ds_read_b96 v[40:42], v39 offset:20480
	s_movk_i32 s14, 0x7f
	v_cmp_lt_u32_e64 s[12:13], 63, v0
	v_sub_u32_e32 v19, v19, v18
	s_waitcnt lgkmcnt(0)
	v_cndmask_b32_e64 v39, 0, v40, s[12:13]
	v_cmp_lt_u32_e64 s[12:13], s14, v0
	v_add_u32_e32 v19, v19, v39
	s_nop 0
	v_cndmask_b32_e64 v40, 0, v41, s[12:13]
	s_movk_i32 s12, 0xbf
	v_cmp_lt_u32_e64 s[12:13], s12, v0
	s_nop 1
	v_cndmask_b32_e64 v41, 0, v42, s[12:13]
	v_add_co_u32_e64 v18, s[12:13], 1, v18
	v_cvt_f32_u32_e32 v18, v18
	v_add3_u32 v19, v19, v40, v41
	v_lshlrev_b32_e32 v40, 2, v0
	v_rsq_f32_e32 v39, v18
	v_add_u32_e32 v18, v19, v30
	ds_write_b32 v40, v18 offset:21504
	v_add_u32_e32 v18, s3, v0
	v_mul_f32_e32 v41, 0x45800000, v39
	s_movk_i32 s3, 0xc4
	v_cndmask_b32_e64 v39, v39, v41, s[12:13]
	v_cmp_gt_u32_e64 s[12:13], s3, v0
	s_mov_b32 s3, 0xc350
	v_cmp_gt_i32_e64 s[14:15], s3, v18
	s_and_b64 s[12:13], s[12:13], s[14:15]
	ds_write2st64_b32 v40, v19, v39 offset0:68 offset1:76
	s_and_b64 exec, exec, s[12:13]
	s_cbranch_execz .LBB1_31
	v_ashrrev_i32_e32 v19, 31, v18
	v_lshl_add_u64 v[18:19], v[18:19], 2, s[30:31]
	global_store_dword v[18:19], v39, off sc0 sc1

.LBB1_37:
	s_or_b64 exec, exec, s[8:9]
	v_lshl_or_b32 v38, v39, 5, v38
	v_ashrrev_i32_e32 v39, 31, v38
	v_lshl_add_u64 v[38:39], v[38:39], 4, s[36:37]
	s_waitcnt lgkmcnt(0)
	global_store_dwordx4 v[38:39], v[18:21], off sc0 sc1
.LBB1_38:
	s_or_b64 exec, exec, s[30:31]
	s_and_saveexec_b64 s[8:9], s[6:7]
	s_cbranch_execz .LBB1_43
	v_mov_b32_e32 v18, 2
	v_lshlrev_b32_sdwa v19, v18, v37 dst_sel:DWORD dst_unused:UNUSED_PAD src0_sel:DWORD src1_sel:WORD_1
	v_mov_b32_e32 v18, 1
	ds_add_rtn_u32 v18, v19, v18 offset:17408
	ds_read_b32 v19, v19 offset:18432
	v_and_b32_e32 v20, 0xffff, v37
	s_movk_i32 s2, 0xfff
	s_waitcnt lgkmcnt(1)
	v_cmp_lt_u32_e64 s[2:3], s2, v18
	s_waitcnt lgkmcnt(0)
	v_lshl_or_b32 v19, v19, 16, v20
	s_and_saveexec_b64 s[6:7], s[2:3]
	s_xor_b64 s[2:3], exec, s[6:7]
	s_cbranch_execz .LBB1_41
	v_add_u32_e32 v20, v18, v30
	v_mov_b32_e32 v21, 0
	v_lshl_add_u64 v[20:21], v[20:21], 2, s[28:29]
	global_store_dword v[20:21], v19, off sc0 sc1

.LBB1_43:
	s_or_b64 exec, exec, s[8:9]
	s_and_saveexec_b64 s[6:7], s[4:5]
	s_cbranch_execz .LBB1_48
	v_mov_b32_e32 v18, 2
	v_lshlrev_b32_sdwa v19, v18, v36 dst_sel:DWORD dst_unused:UNUSED_PAD src0_sel:DWORD src1_sel:WORD_1
	v_mov_b32_e32 v18, 1
	ds_add_rtn_u32 v18, v19, v18 offset:17408
	ds_read_b32 v19, v19 offset:18432
	v_and_b32_e32 v20, 0xffff, v36
	s_movk_i32 s2, 0xfff
	s_waitcnt lgkmcnt(1)
	v_cmp_lt_u32_e64 s[2:3], s2, v18
	s_waitcnt lgkmcnt(0)
	v_lshl_or_b32 v19, v19, 16, v20
	s_and_saveexec_b64 s[4:5], s[2:3]
	s_xor_b64 s[2:3], exec, s[4:5]
	s_cbranch_execz .LBB1_46
	v_add_u32_e32 v20, v18, v30
	v_mov_b32_e32 v21, 0
	v_lshl_add_u64 v[20:21], v[20:21], 2, s[28:29]
	global_store_dword v[20:21], v19, off sc0 sc1

.LBB1_48:
	s_or_b64 exec, exec, s[6:7]
	s_and_saveexec_b64 s[4:5], s[16:17]
	s_cbranch_execz .LBB1_53
	v_mov_b32_e32 v18, 2
	v_lshlrev_b32_sdwa v19, v18, v35 dst_sel:DWORD dst_unused:UNUSED_PAD src0_sel:DWORD src1_sel:WORD_1
	v_mov_b32_e32 v18, 1
	ds_add_rtn_u32 v18, v19, v18 offset:17408
	ds_read_b32 v19, v19 offset:18432
	v_and_b32_e32 v20, 0xffff, v35
	s_movk_i32 s2, 0xfff
	s_waitcnt lgkmcnt(1)
	v_cmp_lt_u32_e64 s[2:3], s2, v18
	s_waitcnt lgkmcnt(0)
	v_lshl_or_b32 v19, v19, 16, v20
	s_and_saveexec_b64 s[6:7], s[2:3]
	s_xor_b64 s[2:3], exec, s[6:7]
	s_cbranch_execz .LBB1_51
	v_add_u32_e32 v20, v18, v30
	v_mov_b32_e32 v21, 0
	v_lshl_add_u64 v[20:21], v[20:21], 2, s[28:29]
	global_store_dword v[20:21], v19, off sc0 sc1

.LBB1_53:
	s_or_b64 exec, exec, s[4:5]
	s_and_saveexec_b64 s[2:3], s[0:1]
	s_cbranch_execz .LBB1_58
	v_mov_b32_e32 v18, 2
	v_lshlrev_b32_sdwa v19, v18, v34 dst_sel:DWORD dst_unused:UNUSED_PAD src0_sel:DWORD src1_sel:WORD_1
	v_mov_b32_e32 v18, 1
	ds_add_rtn_u32 v18, v19, v18 offset:17408
	ds_read_b32 v19, v19 offset:18432
	v_and_b32_e32 v20, 0xffff, v34
	s_movk_i32 s0, 0xfff
	s_waitcnt lgkmcnt(1)
	v_cmp_lt_u32_e64 s[0:1], s0, v18
	s_waitcnt lgkmcnt(0)
	v_lshl_or_b32 v19, v19, 16, v20
	s_and_saveexec_b64 s[4:5], s[0:1]
	s_xor_b64 s[0:1], exec, s[4:5]
	s_cbranch_execz .LBB1_56
	v_add_u32_e32 v20, v18, v30
	v_mov_b32_e32 v21, 0
	v_lshl_add_u64 v[20:21], v[20:21], 2, s[28:29]
	global_store_dword v[20:21], v19, off sc0 sc1

.LBB1_61:
	v_add_u32_e32 v18, v27, v33
	v_lshl_add_u64 v[34:35], v[18:19], 2, s[26:27]
	global_load_dword v34, v[34:35], off
	s_waitcnt vmcnt(0)
	v_lshlrev_b32_sdwa v35, v21, v34 dst_sel:DWORD dst_unused:UNUSED_PAD src0_sel:DWORD src1_sel:WORD_1
	ds_add_rtn_u32 v18, v35, v20 offset:17408
	ds_read_b32 v35, v35 offset:18432
	v_and_b32_e32 v34, 0xffff, v34
	s_waitcnt lgkmcnt(1)
	v_cmp_lt_u32_e32 vcc, s6, v18
	s_waitcnt lgkmcnt(0)
	v_lshl_or_b32 v34, v35, 16, v34
	s_and_saveexec_b64 s[4:5], vcc
	s_xor_b64 s[4:5], exec, s[4:5]
	s_cbranch_execz .LBB1_63
	v_add_u32_e32 v18, v18, v30
	v_lshl_add_u64 v[36:37], v[18:19], 2, s[28:29]
	global_store_dword v[36:37], v34, off sc0 sc1

.LBB1_69:
	ds_read_b32 v27, v21
	v_add_u32_e32 v18, v30, v0
	v_add_u32_e32 v0, 0x400, v0
	v_cmp_ge_u32_e32 vcc, v0, v20
	v_add_u32_e32 v21, 0x1000, v21
	v_lshl_add_u64 v[34:35], v[18:19], 2, s[28:29]
	s_or_b64 s[2:3], vcc, s[2:3]
	s_waitcnt lgkmcnt(0)
	global_store_dword v[34:35], v27, off sc0 sc1
	s_andn2_b64 exec, exec, s[2:3]
	s_cbranch_execnz .LBB1_69
	s_or_b64 exec, exec, s[2:3]

.LBB1_74:
	ds_read_b32 v10, v18 offset:19968
	v_ashrrev_i32_e32 v25, 31, v24
	v_lshlrev_b64 v[12:13], 7, v[24:25]
	s_waitcnt lgkmcnt(0)
	v_mul_f32_e32 v6, v10, v6
	v_mul_f32_e32 v7, v10, v7
	v_mul_f32_e32 v8, v10, v8
	v_mul_f32_e32 v9, v10, v9
	v_cvt_pk_f16_f32 v6, v6, v7
	v_cvt_pk_f16_f32 v7, v8, v9
	v_lshl_add_u64 v[8:9], v[0:1], 0, v[12:13]
	global_store_dwordx2 v[8:9], v[6:7], off sc0 sc1
.LBB1_75:
	s_or_b64 exec, exec, s[0:1]
	s_movk_i32 s0, 0xc40
	v_cmp_gt_u32_e32 vcc, s0, v32
	v_cmp_gt_i32_e64 s[0:1], s2, v22
	s_and_b64 s[0:1], vcc, s[0:1]
	s_and_saveexec_b64 s[2:3], s[0:1]
	s_cbranch_execz .LBB1_77
	v_lshlrev_b32_e32 v6, 2, v23
	ds_read_b32 v6, v6 offset:19456
	v_ashrrev_i32_e32 v23, 31, v22
	v_lshlrev_b64 v[8:9], 7, v[22:23]
	v_lshl_add_u64 v[0:1], v[0:1], 0, v[8:9]
	s_waitcnt lgkmcnt(0)
	v_mul_f32_e32 v2, v6, v2
	v_mul_f32_e32 v3, v6, v3
	v_mul_f32_e32 v4, v6, v4
	v_mul_f32_e32 v5, v6, v5
	v_cvt_pk_f16_f32 v2, v2, v3
	v_cvt_pk_f16_f32 v3, v4, v5
	global_store_dwordx2 v[0:1], v[2:3], off sc0 sc1

.LBB1_78:
	ds_read_b32 v20, v18 offset:19456
	v_ashrrev_i32_e32 v29, 31, v28
	v_lshlrev_b64 v[28:29], 7, v[28:29]
	s_waitcnt lgkmcnt(0)
	v_mul_f32_e32 v14, v20, v14
	v_mul_f32_e32 v15, v20, v15
	v_mul_f32_e32 v16, v20, v16
	v_mul_f32_e32 v17, v20, v17
	v_cvt_pk_f16_f32 v14, v14, v15
	v_cvt_pk_f16_f32 v15, v16, v17
	v_lshl_add_u64 v[16:17], v[0:1], 0, v[28:29]
	global_store_dwordx2 v[16:17], v[14:15], off sc0 sc1
	s_or_b64 exec, exec, s[0:1]
	v_cmp_gt_i32_e32 vcc, s2, v26
	s_and_saveexec_b64 s[0:1], vcc
	s_cbranch_execz .LBB1_73
.LBB1_79:
	ds_read_b32 v14, v18 offset:19712
	v_ashrrev_i32_e32 v27, 31, v26
	v_lshlrev_b64 v[16:17], 7, v[26:27]
	s_waitcnt lgkmcnt(0)
	v_mul_f32_e32 v10, v14, v10
	v_mul_f32_e32 v11, v14, v11
	v_mul_f32_e32 v12, v14, v12
	v_mul_f32_e32 v13, v14, v13
	v_cvt_pk_f16_f32 v10, v10, v11
	v_cvt_pk_f16_f32 v11, v12, v13
	v_lshl_add_u64 v[12:13], v[0:1], 0, v[16:17]
	global_store_dwordx2 v[12:13], v[10:11], off sc0 sc1
	s_or_b64 exec, exec, s[0:1]
	v_cmp_gt_i32_e32 vcc, s2, v24
	s_and_saveexec_b64 s[0:1], vcc
	s_cbranch_execnz .LBB1_74
	s_branch .LBB1_75

.LBB2_28:
	s_or_b64 exec, exec, s[0:1]
	s_waitcnt lgkmcnt(0)
	v_mov_b32_e32 v28, 0
	s_barrier
	ds_read_b128 v[30:33], v28 offset:36096
	v_cmp_eq_u32_e32 vcc, 0, v0
	s_waitcnt lgkmcnt(0)
	v_max_f32_e32 v27, v33, v33
	v_max_f32_e32 v29, v32, v32
	v_max_f32_e32 v27, v29, v27
	v_max3_f32 v27, v30, v31, v27
	s_and_saveexec_b64 s[0:1], vcc
	s_cbranch_execz .LBB2_30
	s_ashr_i32 s21, s20, 31
	s_lshl_b64 s[6:7], s[20:21], 2
	s_add_u32 s6, s22, s6
	s_addc_u32 s7, s23, s7
	v_mul_f32_e32 v29, 0x3b808081, v27
	global_store_dword v28, v29, s[6:7] sc0 sc1
.LBB2_30:
	s_or_b64 exec, exec, s[0:1]
	s_mov_b32 s6, 0x437f0000
	v_div_scale_f32 v28, s[0:1], v27, v27, s6
	v_rcp_f32_e32 v29, v28
	v_div_scale_f32 v30, vcc, s6, v27, s6
	s_movk_i32 s0, 0x90
	v_fma_f32 v31, -v28, v29, 1.0
	v_fmac_f32_e32 v29, v31, v29
	v_mul_f32_e32 v31, v30, v29
	v_fma_f32 v32, -v28, v31, v30
	v_fmac_f32_e32 v31, v32, v29
	v_fma_f32 v28, -v28, v31, v30
	v_div_fmas_f32 v28, v28, v29, v31
	v_div_fixup_f32 v28, v28, v27, s6
	v_cmp_lt_f32_e32 vcc, 0, v27
	s_nop 1
	v_cndmask_b32_e32 v27, 0, v28, vcc
	v_fma_f32 v28, v27, v42, 0.5
	v_fma_f32 v29, v27, v41, 0.5
	v_fma_f32 v30, v27, v40, 0.5
	v_fma_f32 v31, v27, v37, 0.5
	v_cvt_u32_f32_e32 v28, v28
	v_cvt_u32_f32_e32 v29, v29
	v_cvt_u32_f32_e32 v30, v30
	v_cvt_u32_f32_e32 v31, v31
	v_fma_f32 v25, v27, v25, 0.5
	v_fma_f32 v20, v27, v20, 0.5
	v_lshl_or_b32 v28, v30, 8, v28
	v_lshl_or_b32 v29, v31, 8, v29
	v_fma_f32 v30, v27, v36, 0.5
	v_fma_f32 v31, v27, v35, 0.5
	v_cvt_u32_f32_e32 v25, v25
	v_fma_f32 v24, v27, v24, 0.5
	v_cvt_u32_f32_e32 v20, v20
	v_fma_f32 v19, v27, v19, 0.5
	v_fma_f32 v6, v27, v6, 0.5
	v_cvt_u32_f32_e32 v30, v30
	v_cvt_u32_f32_e32 v31, v31
	v_fma_f32 v32, v27, v34, 0.5
	v_fma_f32 v26, v27, v26, 0.5
	v_cvt_u32_f32_e32 v24, v24
	v_cvt_u32_f32_e32 v19, v19
	v_cvt_u32_f32_e32 v6, v6
	v_fma_f32 v4, v27, v4, 0.5
	v_fma_f32 v3, v27, v3, 0.5
	v_cvt_u32_f32_e32 v32, v32
	v_cvt_u32_f32_e32 v26, v26
	v_cvt_u32_f32_e32 v4, v4
	v_cvt_u32_f32_e32 v3, v3
	v_fma_f32 v2, v27, v2, 0.5
	v_cvt_u32_f32_e32 v2, v2
	v_lshl_or_b32 v20, v20, 8, v25
	v_lshl_or_b32 v28, v30, 16, v28
	v_lshl_or_b32 v29, v31, 16, v29
	v_lshl_or_b32 v19, v19, 8, v24
	v_lshl_or_b32 v6, v6, 16, v20
	v_lshl_or_b32 v28, v32, 24, v28
	v_lshl_or_b32 v26, v26, 24, v29
	v_mad_u32_u24 v29, v66, s0, v67
	v_lshl_or_b32 v4, v4, 16, v19
	v_lshl_or_b32 v3, v3, 24, v6
	v_lshl_or_b32 v2, v2, 24, v4
	ds_write2_b32 v29, v28, v3 offset1:2
	v_add_u32_e32 v3, 0x1000, v29
	ds_write2_b32 v3, v26, v2 offset0:128 offset1:130
	v_fma_f32 v2, v27, v5, 0.5
	v_fma_f32 v5, v27, v8, 0.5
	v_cvt_u32_f32_e32 v2, v2
	v_fma_f32 v4, v27, v7, 0.5
	v_cvt_u32_f32_e32 v5, v5
	v_fma_f32 v6, v27, v9, 0.5
	v_fma_f32 v7, v27, v18, 0.5
	v_cvt_u32_f32_e32 v4, v4
	v_cvt_u32_f32_e32 v6, v6
	v_cvt_u32_f32_e32 v7, v7
	v_fma_f32 v8, v27, v12, 0.5
	v_cvt_u32_f32_e32 v8, v8
	v_lshl_or_b32 v2, v5, 8, v2
	v_lshl_or_b32 v4, v6, 8, v4
	v_lshl_or_b32 v2, v7, 16, v2
	v_fma_f32 v5, v27, v10, 0.5
	v_fma_f32 v7, v27, v13, 0.5
	v_fma_f32 v9, v27, v21, 0.5
	v_lshl_or_b32 v4, v8, 16, v4
	v_cvt_u32_f32_e32 v5, v5
	v_fma_f32 v6, v27, v11, 0.5
	v_cvt_u32_f32_e32 v7, v7
	v_fma_f32 v8, v27, v14, 0.5
	v_cvt_u32_f32_e32 v9, v9
	v_fma_f32 v10, v27, v22, 0.5
	v_cvt_u32_f32_e32 v6, v6
	v_cvt_u32_f32_e32 v8, v8
	v_cvt_u32_f32_e32 v10, v10
	v_lshl_or_b32 v2, v5, 24, v2
	v_lshl_or_b32 v5, v9, 8, v7
	v_fma_f32 v7, v27, v15, 0.5
	v_lshl_or_b32 v4, v6, 24, v4
	v_lshl_or_b32 v6, v10, 8, v8
	v_cvt_u32_f32_e32 v7, v7
	v_fma_f32 v8, v27, v16, 0.5
	v_fma_f32 v9, v27, v23, 0.5
	v_cvt_u32_f32_e32 v8, v8
	v_cvt_u32_f32_e32 v9, v9
	v_fma_f32 v10, v27, v17, 0.5
	v_cvt_u32_f32_e32 v10, v10
	v_lshl_or_b32 v5, v7, 16, v5
	s_movk_i32 s0, 0x200
	v_lshl_or_b32 v6, v8, 16, v6
	v_lshl_or_b32 v5, v9, 24, v5
	v_cmp_gt_u32_e32 vcc, s0, v0
	v_lshl_or_b32 v6, v10, 24, v6
	ds_write2_b32 v29, v2, v5 offset0:4 offset1:6
	ds_write2_b32 v3, v4, v6 offset0:132 offset1:134
	s_waitcnt lgkmcnt(0)
	s_barrier
	s_and_saveexec_b64 s[0:1], vcc
	s_cbranch_execz .LBB2_35
	s_mov_b32 s6, 0xc350
	v_cmp_gt_i32_e32 vcc, s6, v72
	s_and_b64 s[2:3], s[2:3], vcc
	s_and_saveexec_b64 s[0:1], s[2:3]
	s_cbranch_execz .LBB2_33
	s_movk_i32 s2, 0x90
	v_mad_u32_u24 v0, v1, s2, v74
	ds_read_b128 v[0:3], v0
	v_ashrrev_i32_e32 v73, 31, v72
	v_lshlrev_b64 v[4:5], 7, v[72:73]
	v_mov_b32_e32 v75, 0
	v_lshl_add_u64 v[4:5], s[10:11], 0, v[4:5]
	v_lshl_add_u64 v[4:5], v[4:5], 0, v[74:75]
	s_waitcnt lgkmcnt(0)
	global_store_dwordx4 v[4:5], v[0:3], off sc0 sc1
.LBB2_33:
	s_or_b64 exec, exec, s[0:1]
	v_cmp_gt_i32_e32 vcc, s6, v70
	s_and_b64 s[0:1], s[4:5], vcc
	s_and_saveexec_b64 s[2:3], s[0:1]
	s_xor_b64 s[2:3], exec, s[2:3]
	s_cbranch_execz .LBB2_35
	s_movk_i32 s0, 0x90
	v_mad_u32_u24 v0, v71, s0, v74
	ds_read_b128 v[0:3], v0
	v_ashrrev_i32_e32 v71, 31, v70
	v_lshlrev_b64 v[4:5], 7, v[70:71]
	v_mov_b32_e32 v75, 0
	v_lshl_add_u64 v[4:5], s[10:11], 0, v[4:5]
	v_lshl_add_u64 v[4:5], v[4:5], 0, v[74:75]
	s_waitcnt lgkmcnt(0)
	global_store_dwordx4 v[4:5], v[0:3], off sc0 sc1
